# speedup vs baseline: 1.0073x; 1.0073x over previous
_Z10attn64_fwdPKDF16_S0_S0_PDF16_:
	v_readfirstlane_b32 s3, v0
	s_cmpk_lt_i32 s3, 0x100
	s_cbranch_scc0 .LBB1_2
	s_setprio 1
